# speedup vs baseline: 1.0135x; 1.0080x over previous
.LBB2_36:
	s_or_b64 exec, exec, s[12:13]
	v_mbcnt_lo_u32_b32 v5, -1, 0
	v_mbcnt_hi_u32_b32 v5, -1, v5
	v_and_b32_e32 v6, 64, v5
	v_add_u32_e32 v7, -1, v5
	v_cmp_lt_i32_e64 s[12:13], v7, v6
	v_and_b32_e32 v11, 63, v0
	v_add_u32_e32 v12, -2, v5
	v_cndmask_b32_e64 v7, v7, v5, s[12:13]
	v_lshlrev_b32_e32 v7, 2, v7
	ds_bpermute_b32 v7, v7, v10
	v_cmp_ne_u32_e64 s[12:13], 0, v11
	s_load_dwordx2 s[20:21], s[0:1], 0x18
	s_waitcnt lgkmcnt(0)
	v_cndmask_b32_e64 v7, 0, v7, s[12:13]
	v_cmp_lt_i32_e64 s[12:13], v12, v6
	v_add_u32_e32 v7, v7, v10
	s_nop 0
	v_cndmask_b32_e64 v12, v12, v5, s[12:13]
	v_lshlrev_b32_e32 v12, 2, v12
	ds_bpermute_b32 v12, v12, v7
	v_cmp_lt_u32_e64 s[12:13], 1, v11
	s_waitcnt lgkmcnt(0)
	s_nop 0
	v_cndmask_b32_e64 v12, 0, v12, s[12:13]
	v_add_u32_e32 v7, v12, v7
	v_add_u32_e32 v12, -4, v5
	v_cmp_lt_i32_e64 s[12:13], v12, v6
	s_nop 1
	v_cndmask_b32_e64 v12, v12, v5, s[12:13]
	v_lshlrev_b32_e32 v12, 2, v12
	ds_bpermute_b32 v12, v12, v7
	v_cmp_lt_u32_e64 s[12:13], 3, v11
	s_waitcnt lgkmcnt(0)
	s_nop 0
	v_cndmask_b32_e64 v12, 0, v12, s[12:13]
	v_add_u32_e32 v7, v12, v7
	v_add_u32_e32 v12, -8, v5
	v_cmp_lt_i32_e64 s[12:13], v12, v6
	s_nop 1
	v_cndmask_b32_e64 v12, v12, v5, s[12:13]
	v_lshlrev_b32_e32 v12, 2, v12
	ds_bpermute_b32 v12, v12, v7
	v_cmp_lt_u32_e64 s[12:13], 7, v11
	s_waitcnt lgkmcnt(0)
	s_nop 0
	v_cndmask_b32_e64 v12, 0, v12, s[12:13]
	v_add_u32_e32 v7, v12, v7
	v_add_u32_e32 v12, -16, v5
	v_cmp_lt_i32_e64 s[12:13], v12, v6
	s_nop 1
	v_cndmask_b32_e64 v12, v12, v5, s[12:13]
	v_lshlrev_b32_e32 v12, 2, v12
	ds_bpermute_b32 v12, v12, v7
	v_cmp_lt_u32_e64 s[12:13], 15, v11
	s_waitcnt lgkmcnt(0)
	s_nop 0
	v_cndmask_b32_e64 v12, 0, v12, s[12:13]
	v_add_u32_e32 v12, v12, v7
	v_subrev_u32_e32 v7, 32, v5
	v_cmp_lt_i32_e64 s[12:13], v7, v6
	s_nop 1
	v_cndmask_b32_e64 v5, v7, v5, s[12:13]
	v_lshlrev_b32_e32 v5, 2, v5
	ds_bpermute_b32 v5, v5, v12
	v_cmp_lt_u32_e64 s[12:13], 31, v11
	v_lshrrev_b32_e32 v7, 6, v0
	s_waitcnt lgkmcnt(0)
	v_cndmask_b32_e64 v5, 0, v5, s[12:13]
	v_add_u32_e32 v6, v5, v12
	v_cmp_eq_u32_e64 s[12:13], 63, v11
	s_and_saveexec_b64 s[24:25], s[12:13]
	v_lshlrev_b32_e32 v5, 2, v7
	ds_write_b32 v5, v6 offset:5888
	s_or_b64 exec, exec, s[24:25]
	v_mov_b32_e32 v5, 0
	s_waitcnt lgkmcnt(0)
	s_barrier
	ds_read_b128 v[12:15], v5 offset:5888
	ds_read_b128 v[16:19], v5 offset:5904
	ds_read_b128 v[20:23], v5 offset:5920
	ds_read_b96 v[24:26], v5 offset:5936
	v_cmp_lt_u32_e64 s[12:13], 63, v0
	s_waitcnt lgkmcnt(0)
	s_barrier
	v_cndmask_b32_e64 v11, 0, v12, s[12:13]
	s_movk_i32 s12, 0x7f
	v_cmp_lt_u32_e64 s[12:13], s12, v0
	s_nop 1
	v_cndmask_b32_e64 v12, 0, v13, s[12:13]
	s_movk_i32 s12, 0xbf
	v_cmp_lt_u32_e64 s[12:13], s12, v0
	s_nop 1
	v_cndmask_b32_e64 v13, 0, v14, s[12:13]
	s_movk_i32 s12, 0xff
	v_cmp_lt_u32_e64 s[12:13], s12, v0
	s_nop 1
	v_cndmask_b32_e64 v14, 0, v15, s[12:13]
	s_movk_i32 s12, 0x13f
	v_cmp_lt_u32_e64 s[12:13], s12, v0
	s_nop 1
	v_cndmask_b32_e64 v15, 0, v16, s[12:13]
	s_movk_i32 s12, 0x17f
	v_cmp_lt_u32_e64 s[12:13], s12, v0
	s_nop 1
	v_cndmask_b32_e64 v16, 0, v17, s[12:13]
	s_movk_i32 s12, 0x1bf
	v_cmp_lt_u32_e64 s[12:13], s12, v0
	s_nop 1
	v_cndmask_b32_e64 v17, 0, v18, s[12:13]
	s_movk_i32 s12, 0x1ff
	v_cmp_lt_u32_e64 s[12:13], s12, v0
	s_nop 1
	v_cndmask_b32_e64 v18, 0, v19, s[12:13]
	s_movk_i32 s12, 0x23f
	v_cmp_lt_u32_e64 s[12:13], s12, v0
	s_nop 1
	v_cndmask_b32_e64 v19, 0, v20, s[12:13]
	s_movk_i32 s12, 0x27f
	v_cmp_lt_u32_e64 s[12:13], s12, v0
	s_nop 1
	v_cndmask_b32_e64 v20, 0, v21, s[12:13]
	s_movk_i32 s12, 0x2bf
	v_cmp_lt_u32_e64 s[12:13], s12, v0
	s_nop 1
	v_cndmask_b32_e64 v21, 0, v22, s[12:13]
	s_movk_i32 s12, 0x2ff
	v_cmp_lt_u32_e64 s[12:13], s12, v0
	s_nop 1
	v_cndmask_b32_e64 v22, 0, v23, s[12:13]
	s_movk_i32 s12, 0x33f
	v_cmp_lt_u32_e64 s[12:13], s12, v0
	s_nop 1
	v_cndmask_b32_e64 v23, 0, v24, s[12:13]
	s_movk_i32 s12, 0x37f
	v_cmp_lt_u32_e64 s[12:13], s12, v0
	s_nop 1
	v_cndmask_b32_e64 v24, 0, v25, s[12:13]
	v_cmp_eq_u32_e64 s[12:13], 15, v7
	s_nop 1
	v_cndmask_b32_e64 v7, 0, v26, s[12:13]
	s_add_i32 s12, s16, s26
	v_sub_u32_e32 v25, s12, v10
	v_add3_u32 v6, v25, v6, v11
	v_add3_u32 v6, v6, v12, v13
	v_add3_u32 v6, v6, v14, v15
	v_add3_u32 v6, v6, v16, v17
	v_add3_u32 v6, v6, v18, v19
	v_add3_u32 v6, v6, v20, v21
	v_add3_u32 v6, v6, v22, v23
	v_add3_u32 v6, v6, v24, v7
	s_add_i32 s44, s16, s26
	s_and_saveexec_b64 s[24:25], s[22:23]
	s_cbranch_execz .LBB2_41
	s_load_dwordx2 s[22:23], s[0:1], 0x10
	v_ashrrev_i32_e32 v7, 31, v6
	s_mov_b32 s12, 0x1869f
	v_lshl_add_u64 v[12:13], v[6:7], 2, s[20:21]
	global_store_dword v[12:13], v4, off
	v_subrev_u32_e32 v28, s44, v6
	v_lshlrev_b32_e32 v28, 2, v28
	ds_write_b32 v28, v4 offset:38720
	s_waitcnt lgkmcnt(0)
	v_lshl_add_u64 v[12:13], v[4:5], 2, s[22:23]
	v_cmp_eq_u32_e64 s[12:13], s12, v4
	global_store_dword v[12:13], v6, off
	s_and_b64 exec, exec, s[12:13]
	s_cbranch_execz .LBB2_41
	v_add_u32_e32 v4, v6, v10
	v_mov_b32_e32 v5, 0x61000
	global_store_dword v5, v4, s[22:23] offset:2688
.LBB2_41:
	s_or_b64 exec, exec, s[24:25]
	s_and_saveexec_b64 s[12:13], vcc
	v_lshlrev_b32_e32 v4, 2, v0
	v_add_u32_e32 v5, 1, v6
	ds_write_b32 v4, v5 offset:4864
	s_or_b64 exec, exec, s[12:13]
	s_waitcnt lgkmcnt(0)
	s_barrier
	s_sub_i32 s45, s17, s16
	s_cmpk_gt_i32 s45, 0x1400
	s_cbranch_scc1 .Lc6_fallback
	v_mov_b32_e32 v29, 1
	v_mov_b32_e32 v28, 2
	s_mov_b64 exec, s[10:11]
	v_lshlrev_b32_sdwa v32, v28, v9 dst_sel:DWORD dst_unused:UNUSED_PAD src0_sel:DWORD src1_sel:BYTE_0
	ds_add_rtn_u32 v32, v32, v29 offset:4864
	s_mov_b64 exec, s[8:9]
	v_lshlrev_b32_sdwa v33, v28, v8 dst_sel:DWORD dst_unused:UNUSED_PAD src0_sel:DWORD src1_sel:BYTE_0
	ds_add_rtn_u32 v33, v33, v29 offset:4864
	s_mov_b64 exec, s[6:7]
	v_lshlrev_b32_sdwa v34, v28, v3 dst_sel:DWORD dst_unused:UNUSED_PAD src0_sel:DWORD src1_sel:BYTE_0
	ds_add_rtn_u32 v34, v34, v29 offset:4864
	s_mov_b64 exec, s[4:5]
	v_lshlrev_b32_sdwa v35, v28, v1 dst_sel:DWORD dst_unused:UNUSED_PAD src0_sel:DWORD src1_sel:BYTE_0
	ds_add_rtn_u32 v35, v35, v29 offset:4864
	s_mov_b64 exec, s[40:41]
	v_lshlrev_b32_sdwa v36, v28, v27 dst_sel:DWORD dst_unused:UNUSED_PAD src0_sel:DWORD src1_sel:BYTE_0
	ds_add_rtn_u32 v36, v36, v29 offset:4864
	s_mov_b64 exec, -1
	v_lshrrev_b32_e32 v40, 8, v9
	v_lshrrev_b32_e32 v41, 8, v8
	v_lshrrev_b32_e32 v42, 8, v3
	v_lshrrev_b32_e32 v43, 8, v1
	v_lshrrev_b32_e32 v44, 8, v27
	s_waitcnt lgkmcnt(0)
	v_subrev_u32_e32 v32, s44, v32
	v_lshlrev_b32_e32 v32, 2, v32
	v_subrev_u32_e32 v33, s44, v33
	v_lshlrev_b32_e32 v33, 2, v33
	v_subrev_u32_e32 v34, s44, v34
	v_lshlrev_b32_e32 v34, 2, v34
	v_subrev_u32_e32 v35, s44, v35
	v_lshlrev_b32_e32 v35, 2, v35
	v_subrev_u32_e32 v36, s44, v36
	v_lshlrev_b32_e32 v36, 2, v36
	s_mov_b64 exec, s[10:11]
	ds_write_b32 v32, v40 offset:38720
	s_mov_b64 exec, s[8:9]
	ds_write_b32 v33, v41 offset:38720
	s_mov_b64 exec, s[6:7]
	ds_write_b32 v34, v42 offset:38720
	s_mov_b64 exec, s[4:5]
	ds_write_b32 v35, v43 offset:38720
	s_mov_b64 exec, s[40:41]
	ds_write_b32 v36, v44 offset:38720
	s_mov_b64 exec, -1
	s_sub_i32 s46, 0x186a0, s26
	s_min_i32 s46, s46, 0x100
	s_add_i32 s45, s45, s46
	s_mov_b32 s46, s44
	s_mov_b32 s47, 0
	s_lshl_b64 s[46:47], s[46:47], 2
	s_add_u32 s46, s20, s46
	s_addc_u32 s47, s21, s47
	v_lshlrev_b32_e32 v29, 2, v0
	s_waitcnt lgkmcnt(0)
	s_barrier
	ds_read_b32 v32, v29 offset:38720
	ds_read_b32 v33, v29 offset:42816
	ds_read_b32 v34, v29 offset:46912
	ds_read_b32 v35, v29 offset:51008
	ds_read_b32 v36, v29 offset:55104
	ds_read_b32 v37, v29 offset:59200
	s_waitcnt lgkmcnt(0)
	v_cmp_gt_i32_e64 s[50:51], s45, v0
	s_and_saveexec_b64 s[42:43], s[50:51]
	global_store_dword v29, v32, s[46:47]
	s_mov_b64 exec, s[42:43]
	v_add_u32_e32 v30, 0x400, v0
	v_add_u32_e32 v31, 0x1000, v29
	v_cmp_gt_i32_e64 s[50:51], s45, v30
	s_and_saveexec_b64 s[42:43], s[50:51]
	global_store_dword v31, v33, s[46:47]
	s_mov_b64 exec, s[42:43]
	v_add_u32_e32 v30, 0x800, v0
	v_add_u32_e32 v31, 0x2000, v29
	v_cmp_gt_i32_e64 s[50:51], s45, v30
	s_and_saveexec_b64 s[42:43], s[50:51]
	global_store_dword v31, v34, s[46:47]
	s_mov_b64 exec, s[42:43]
	v_add_u32_e32 v30, 0xc00, v0
	v_add_u32_e32 v31, 0x3000, v29
	v_cmp_gt_i32_e64 s[50:51], s45, v30
	s_and_saveexec_b64 s[42:43], s[50:51]
	global_store_dword v31, v35, s[46:47]
	s_mov_b64 exec, s[42:43]
	v_add_u32_e32 v30, 0x1000, v0
	v_add_u32_e32 v31, 0x4000, v29
	v_cmp_gt_i32_e64 s[50:51], s45, v30
	s_and_saveexec_b64 s[42:43], s[50:51]
	global_store_dword v31, v36, s[46:47]
	s_mov_b64 exec, s[42:43]
	v_add_u32_e32 v30, 0x1400, v0
	v_add_u32_e32 v31, 0x5000, v29
	v_cmp_gt_i32_e64 s[50:51], s45, v30
	s_and_saveexec_b64 s[42:43], s[50:51]
	global_store_dword v31, v37, s[46:47]
	s_mov_b64 exec, s[42:43]
	s_branch .LBB2_74
.Lc6_fallback:
	s_and_saveexec_b64 s[12:13], s[10:11]
	s_cbranch_execnz .LBB2_52
	s_or_b64 exec, exec, s[12:13]
	s_and_saveexec_b64 s[10:11], s[8:9]
	s_cbranch_execnz .LBB2_53

	.amdhsa_kernel _Z5k_csrPKiS0_PiS1_PKfS3_S3_S3_PDF16_P15HIP_vector_typeIfLj4EES7_
		.amdhsa_group_segment_fixed_size 60224
		.amdhsa_private_segment_fixed_size 0
		.amdhsa_kernarg_size 88
		.amdhsa_user_sgpr_count 2
		.amdhsa_user_sgpr_dispatch_ptr 0
		.amdhsa_user_sgpr_queue_ptr 0
		.amdhsa_user_sgpr_kernarg_segment_ptr 1
		.amdhsa_user_sgpr_dispatch_id 0
		.amdhsa_user_sgpr_kernarg_preload_length 0
		.amdhsa_user_sgpr_kernarg_preload_offset 0
		.amdhsa_user_sgpr_private_segment_size 0
		.amdhsa_uses_dynamic_stack 0
		.amdhsa_enable_private_segment 0
		.amdhsa_system_sgpr_workgroup_id_x 1
		.amdhsa_system_sgpr_workgroup_id_y 0
		.amdhsa_system_sgpr_workgroup_id_z 0
		.amdhsa_system_sgpr_workgroup_info 0
		.amdhsa_system_vgpr_workitem_id 0
		.amdhsa_next_free_vgpr 64
		.amdhsa_next_free_sgpr 80
		.amdhsa_accum_offset 64
		.amdhsa_reserve_vcc 1
		.amdhsa_float_round_mode_32 0
		.amdhsa_float_round_mode_16_64 0
		.amdhsa_float_denorm_mode_32 3
		.amdhsa_float_denorm_mode_16_64 3
		.amdhsa_dx10_clamp 1
		.amdhsa_ieee_mode 1
		.amdhsa_fp16_overflow 0
		.amdhsa_tg_split 0
		.amdhsa_exception_fp_ieee_invalid_op 0
		.amdhsa_exception_fp_denorm_src 0
		.amdhsa_exception_fp_ieee_div_zero 0
		.amdhsa_exception_fp_ieee_overflow 0
		.amdhsa_exception_fp_ieee_underflow 0
		.amdhsa_exception_fp_ieee_inexact 0
		.amdhsa_exception_int_div_zero 0
	.end_amdhsa_kernel

amdhsa.kernels:
  - .agpr_count:     0
    .args:
      - .actual_access:  read_only
        .address_space:  global
        .offset:         0
        .size:           8
        .value_kind:     global_buffer
      - .actual_access:  write_only
        .address_space:  global
        .offset:         8
        .size:           8
        .value_kind:     global_buffer
      - .actual_access:  read_only
        .address_space:  global
        .offset:         16
        .size:           8
        .value_kind:     global_buffer
      - .actual_access:  read_only
        .address_space:  global
        .offset:         24
        .size:           8
        .value_kind:     global_buffer
      - .actual_access:  read_only
        .address_space:  global
        .offset:         32
        .size:           8
        .value_kind:     global_buffer
      - .actual_access:  read_only
        .address_space:  global
        .offset:         40
        .size:           8
        .value_kind:     global_buffer
      - .actual_access:  read_only
        .address_space:  global
        .offset:         48
        .size:           8
        .value_kind:     global_buffer
      - .actual_access:  read_only
        .address_space:  global
        .offset:         56
        .size:           8
        .value_kind:     global_buffer
      - .actual_access:  read_only
        .address_space:  global
        .offset:         64
        .size:           8
        .value_kind:     global_buffer
      - .actual_access:  read_only
        .address_space:  global
        .offset:         72
        .size:           8
        .value_kind:     global_buffer
      - .actual_access:  read_only
        .address_space:  global
        .offset:         80
        .size:           8
        .value_kind:     global_buffer
      - .actual_access:  write_only
        .address_space:  global
        .offset:         88
        .size:           8
        .value_kind:     global_buffer
      - .actual_access:  write_only
        .address_space:  global
        .offset:         96
        .size:           8
        .value_kind:     global_buffer
      - .actual_access:  write_only
        .address_space:  global
        .offset:         104
        .size:           8
        .value_kind:     global_buffer
      - .actual_access:  write_only
        .address_space:  global
        .offset:         112
        .size:           8
        .value_kind:     global_buffer
      - .actual_access:  write_only
        .address_space:  global
        .offset:         120
        .size:           8
        .value_kind:     global_buffer
    .group_segment_fixed_size: 1564
    .kernarg_segment_align: 8
    .kernarg_segment_size: 128
    .language:       OpenCL C
    .language_version:
      - 2
      - 0
    .max_flat_workgroup_size: 1024
    .name:           _Z6k_pre1PKiPiPKfS3_S3_S3_S3_S3_S3_S3_S3_PDF16_S4_S4_PfS5_
    .private_segment_fixed_size: 0
    .sgpr_count:     26
    .sgpr_spill_count: 0
    .symbol:         _Z6k_pre1PKiPiPKfS3_S3_S3_S3_S3_S3_S3_S3_PDF16_S4_S4_PfS5_.kd
    .uniform_work_group_size: 1
    .uses_dynamic_stack: false
    .vgpr_count:     64
    .vgpr_spill_count: 0
    .wavefront_size: 64
  - .agpr_count:     0
    .args:
      - .actual_access:  read_only
        .address_space:  global
        .offset:         0
        .size:           8
        .value_kind:     global_buffer
      - .actual_access:  read_only
        .address_space:  global
        .offset:         8
        .size:           8
        .value_kind:     global_buffer
      - .actual_access:  read_only
        .address_space:  global
        .offset:         16
        .size:           8
        .value_kind:     global_buffer
      - .actual_access:  read_only
        .address_space:  global
        .offset:         24
        .size:           8
        .value_kind:     global_buffer
      - .actual_access:  write_only
        .address_space:  global
        .offset:         32
        .size:           8
        .value_kind:     global_buffer
      - .actual_access:  write_only
        .address_space:  global
        .offset:         40
        .size:           8
        .value_kind:     global_buffer
    .group_segment_fixed_size: 1632
    .kernarg_segment_align: 8
    .kernarg_segment_size: 48
    .language:       OpenCL C
    .language_version:
      - 2
      - 0
    .max_flat_workgroup_size: 1024
    .name:           _Z9k_scatterPKiS0_S0_S0_PiS1_
    .private_segment_fixed_size: 0
    .sgpr_count:     22
    .sgpr_spill_count: 0
    .symbol:         _Z9k_scatterPKiS0_S0_S0_PiS1_.kd
    .uniform_work_group_size: 1
    .uses_dynamic_stack: false
    .vgpr_count:     50
    .vgpr_spill_count: 0
    .wavefront_size: 64
  - .agpr_count:     0
    .args:
      - .actual_access:  read_only
        .address_space:  global
        .offset:         0
        .size:           8
        .value_kind:     global_buffer
      - .actual_access:  read_only
        .address_space:  global
        .offset:         8
        .size:           8
        .value_kind:     global_buffer
      - .actual_access:  write_only
        .address_space:  global
        .offset:         16
        .size:           8
        .value_kind:     global_buffer
      - .actual_access:  write_only
        .address_space:  global
        .offset:         24
        .size:           8
        .value_kind:     global_buffer
      - .actual_access:  read_only
        .address_space:  global
        .offset:         32
        .size:           8
        .value_kind:     global_buffer
      - .actual_access:  read_only
        .address_space:  global
        .offset:         40
        .size:           8
        .value_kind:     global_buffer
      - .actual_access:  read_only
        .address_space:  global
        .offset:         48
        .size:           8
        .value_kind:     global_buffer
      - .actual_access:  read_only
        .address_space:  global
        .offset:         56
        .size:           8
        .value_kind:     global_buffer
      - .actual_access:  write_only
        .address_space:  global
        .offset:         64
        .size:           8
        .value_kind:     global_buffer
      - .actual_access:  write_only
        .address_space:  global
        .offset:         72
        .size:           8
        .value_kind:     global_buffer
      - .actual_access:  write_only
        .address_space:  global
        .offset:         80
        .size:           8
        .value_kind:     global_buffer
    .group_segment_fixed_size: 60224
    .kernarg_segment_align: 8
    .kernarg_segment_size: 88
    .language:       OpenCL C
    .language_version:
      - 2
      - 0
    .max_flat_workgroup_size: 1024
    .name:           _Z5k_csrPKiS0_PiS1_PKfS3_S3_S3_PDF16_P15HIP_vector_typeIfLj4EES7_
    .private_segment_fixed_size: 0
    .sgpr_count:     86
    .sgpr_spill_count: 0
    .symbol:         _Z5k_csrPKiS0_PiS1_PKfS3_S3_S3_PDF16_P15HIP_vector_typeIfLj4EES7_.kd
    .uniform_work_group_size: 1
    .uses_dynamic_stack: false
    .vgpr_count:     64
    .vgpr_spill_count: 0
    .wavefront_size: 64
  - .agpr_count:     0
    .args:
      - .actual_access:  read_only
        .address_space:  global
        .offset:         0
        .size:           8
        .value_kind:     global_buffer
      - .actual_access:  write_only
        .address_space:  global
        .offset:         8
        .size:           8
        .value_kind:     global_buffer
      - .actual_access:  write_only
        .address_space:  global
        .offset:         16
        .size:           8
        .value_kind:     global_buffer
    .group_segment_fixed_size: 16
    .kernarg_segment_align: 8
    .kernarg_segment_size: 24
    .language:       OpenCL C
    .language_version:
      - 2
      - 0
    .max_flat_workgroup_size: 256
    .name:           _Z6k_pre2PKiPiS1_
    .private_segment_fixed_size: 0
    .sgpr_count:     14
    .sgpr_spill_count: 0
    .symbol:         _Z6k_pre2PKiPiS1_.kd
    .uniform_work_group_size: 1
    .uses_dynamic_stack: false
    .vgpr_count:     14
    .vgpr_spill_count: 0
    .wavefront_size: 64
  - .agpr_count:     0
    .args:
      - .actual_access:  read_only
        .address_space:  global
        .offset:         0
        .size:           8
        .value_kind:     global_buffer
      - .actual_access:  read_only
        .address_space:  global
        .offset:         8
        .size:           8
        .value_kind:     global_buffer
      - .actual_access:  read_only
        .address_space:  global
        .offset:         16
        .size:           8
        .value_kind:     global_buffer
      - .actual_access:  read_only
        .address_space:  global
        .offset:         24
        .size:           8
        .value_kind:     global_buffer
      - .actual_access:  read_only
        .address_space:  global
        .offset:         32
        .size:           8
        .value_kind:     global_buffer
      - .actual_access:  write_only
        .address_space:  global
        .offset:         40
        .size:           8
        .value_kind:     global_buffer
    .group_segment_fixed_size: 1408
    .kernarg_segment_align: 8
    .kernarg_segment_size: 48
    .language:       OpenCL C
    .language_version:
      - 2
      - 0
    .max_flat_workgroup_size: 256
    .name:           _Z7k_finalPKfS0_S0_S0_S0_Pf
    .private_segment_fixed_size: 0
    .sgpr_count:     26
    .sgpr_spill_count: 0
    .symbol:         _Z7k_finalPKfS0_S0_S0_S0_Pf.kd
    .uniform_work_group_size: 1
    .uses_dynamic_stack: false
    .vgpr_count:     96
    .vgpr_spill_count: 0
    .wavefront_size: 64
  - .agpr_count:     0
    .args:
      - .actual_access:  read_only
        .address_space:  global
        .offset:         0
        .size:           8
        .value_kind:     global_buffer
      - .actual_access:  read_only
        .address_space:  global
        .offset:         8
        .size:           8
        .value_kind:     global_buffer
      - .actual_access:  read_only
        .address_space:  global
        .offset:         16
        .size:           8
        .value_kind:     global_buffer
      - .actual_access:  read_only
        .address_space:  global
        .offset:         24
        .size:           8
        .value_kind:     global_buffer
      - .actual_access:  read_only
        .address_space:  global
        .offset:         32
        .size:           8
        .value_kind:     global_buffer
      - .actual_access:  read_only
        .address_space:  global
        .offset:         40
        .size:           8
        .value_kind:     global_buffer
      - .actual_access:  read_only
        .address_space:  global
        .offset:         48
        .size:           8
        .value_kind:     global_buffer
      - .actual_access:  read_only
        .address_space:  global
        .offset:         56
        .size:           8
        .value_kind:     global_buffer
      - .actual_access:  write_only
        .address_space:  global
        .offset:         64
        .size:           8
        .value_kind:     global_buffer
      - .actual_access:  write_only
        .address_space:  global
        .offset:         72
        .size:           8
        .value_kind:     global_buffer
      - .actual_access:  write_only
        .address_space:  global
        .offset:         80
        .size:           8
        .value_kind:     global_buffer
      - .actual_access:  read_only
        .address_space:  global
        .offset:         88
        .size:           8
        .value_kind:     global_buffer
      - .actual_access:  read_only
        .address_space:  global
        .offset:         96
        .size:           8
        .value_kind:     global_buffer
      - .actual_access:  read_only
        .address_space:  global
        .offset:         104
        .size:           8
        .value_kind:     global_buffer
      - .actual_access:  read_only
        .address_space:  global
        .offset:         112
        .size:           8
        .value_kind:     global_buffer
      - .actual_access:  read_only
        .address_space:  global
        .offset:         120
        .size:           8
        .value_kind:     global_buffer
      - .actual_access:  read_only
        .address_space:  global
        .offset:         128
        .size:           8
        .value_kind:     global_buffer
      - .actual_access:  read_only
        .address_space:  global
        .offset:         136
        .size:           8
        .value_kind:     global_buffer
      - .actual_access:  read_only
        .address_space:  global
        .offset:         144
        .size:           8
        .value_kind:     global_buffer
    .group_segment_fixed_size: 29248
    .kernarg_segment_align: 8
    .kernarg_segment_size: 152
    .language:       OpenCL C
    .language_version:
      - 2
      - 0
    .max_flat_workgroup_size: 256
    .name:           _Z7k_layerILi0EEvPKiS1_PKfS3_PKDF16_S3_S5_S5_PDF16_P15HIP_vector_typeIfLj4EES9_S3_S3_S3_S3_S3_S3_PfSA_
    .private_segment_fixed_size: 0
    .sgpr_count:     66
    .sgpr_spill_count: 0
    .symbol:         _Z7k_layerILi0EEvPKiS1_PKfS3_PKDF16_S3_S5_S5_PDF16_P15HIP_vector_typeIfLj4EES9_S3_S3_S3_S3_S3_S3_PfSA_.kd
    .uniform_work_group_size: 1
    .uses_dynamic_stack: false
    .vgpr_count:     86
    .vgpr_spill_count: 0
    .wavefront_size: 64
  - .agpr_count:     0
    .args:
      - .actual_access:  read_only
        .address_space:  global
        .offset:         0
        .size:           8
        .value_kind:     global_buffer
      - .actual_access:  read_only
        .address_space:  global
        .offset:         8
        .size:           8
        .value_kind:     global_buffer
      - .actual_access:  read_only
        .address_space:  global
        .offset:         16
        .size:           8
        .value_kind:     global_buffer
      - .actual_access:  read_only
        .address_space:  global
        .offset:         24
        .size:           8
        .value_kind:     global_buffer
      - .actual_access:  read_only
        .address_space:  global
        .offset:         32
        .size:           8
        .value_kind:     global_buffer
      - .actual_access:  read_only
        .address_space:  global
        .offset:         40
        .size:           8
        .value_kind:     global_buffer
      - .actual_access:  read_only
        .address_space:  global
        .offset:         48
        .size:           8
        .value_kind:     global_buffer
      - .actual_access:  read_only
        .address_space:  global
        .offset:         56
        .size:           8
        .value_kind:     global_buffer
      - .actual_access:  write_only
        .address_space:  global
        .offset:         64
        .size:           8
        .value_kind:     global_buffer
      - .actual_access:  write_only
        .address_space:  global
        .offset:         72
        .size:           8
        .value_kind:     global_buffer
      - .actual_access:  write_only
        .address_space:  global
        .offset:         80
        .size:           8
        .value_kind:     global_buffer
      - .actual_access:  read_only
        .address_space:  global
        .offset:         88
        .size:           8
        .value_kind:     global_buffer
      - .actual_access:  read_only
        .address_space:  global
        .offset:         96
        .size:           8
        .value_kind:     global_buffer
      - .actual_access:  read_only
        .address_space:  global
        .offset:         104
        .size:           8
        .value_kind:     global_buffer
      - .actual_access:  read_only
        .address_space:  global
        .offset:         112
        .size:           8
        .value_kind:     global_buffer
      - .actual_access:  read_only
        .address_space:  global
        .offset:         120
        .size:           8
        .value_kind:     global_buffer
      - .actual_access:  read_only
        .address_space:  global
        .offset:         128
        .size:           8
        .value_kind:     global_buffer
      - .actual_access:  read_only
        .address_space:  global
        .offset:         136
        .size:           8
        .value_kind:     global_buffer
      - .actual_access:  read_only
        .address_space:  global
        .offset:         144
        .size:           8
        .value_kind:     global_buffer
    .group_segment_fixed_size: 21504
    .kernarg_segment_align: 8
    .kernarg_segment_size: 152
    .language:       OpenCL C
    .language_version:
      - 2
      - 0
    .max_flat_workgroup_size: 256
    .name:           _Z7k_layerILi1EEvPKiS1_PKfS3_PKDF16_S3_S5_S5_PDF16_P15HIP_vector_typeIfLj4EES9_S3_S3_S3_S3_S3_S3_PfSA_
    .private_segment_fixed_size: 0
    .sgpr_count:     70
    .sgpr_spill_count: 0
    .symbol:         _Z7k_layerILi1EEvPKiS1_PKfS3_PKDF16_S3_S5_S5_PDF16_P15HIP_vector_typeIfLj4EES9_S3_S3_S3_S3_S3_S3_PfSA_.kd
    .uniform_work_group_size: 1
    .uses_dynamic_stack: false
    .vgpr_count:     96
    .vgpr_spill_count: 0
    .wavefront_size: 64
  - .agpr_count:     0
    .args:
      - .actual_access:  read_only
        .address_space:  global
        .offset:         0
        .size:           8
        .value_kind:     global_buffer
      - .actual_access:  read_only
        .address_space:  global
        .offset:         8
        .size:           8
        .value_kind:     global_buffer
      - .actual_access:  read_only
        .address_space:  global
        .offset:         16
        .size:           8
        .value_kind:     global_buffer
      - .actual_access:  read_only
        .address_space:  global
        .offset:         24
        .size:           8
        .value_kind:     global_buffer
      - .actual_access:  read_only
        .address_space:  global
        .offset:         32
        .size:           8
        .value_kind:     global_buffer
      - .actual_access:  read_only
        .address_space:  global
        .offset:         40
        .size:           8
        .value_kind:     global_buffer
      - .actual_access:  read_only
        .address_space:  global
        .offset:         48
        .size:           8
        .value_kind:     global_buffer
      - .actual_access:  read_only
        .address_space:  global
        .offset:         56
        .size:           8
        .value_kind:     global_buffer
      - .actual_access:  read_only
        .address_space:  global
        .offset:         64
        .size:           8
        .value_kind:     global_buffer
      - .actual_access:  read_only
        .address_space:  global
        .offset:         72
        .size:           8
        .value_kind:     global_buffer
      - .actual_access:  read_only
        .address_space:  global
        .offset:         80
        .size:           8
        .value_kind:     global_buffer
      - .actual_access:  read_only
        .address_space:  global
        .offset:         88
        .size:           8
        .value_kind:     global_buffer
      - .actual_access:  read_only
        .address_space:  global
        .offset:         96
        .size:           8
        .value_kind:     global_buffer
      - .actual_access:  read_only
        .address_space:  global
        .offset:         104
        .size:           8
        .value_kind:     global_buffer
      - .actual_access:  read_only
        .address_space:  global
        .offset:         112
        .size:           8
        .value_kind:     global_buffer
      - .actual_access:  read_only
        .address_space:  global
        .offset:         120
        .size:           8
        .value_kind:     global_buffer
      - .actual_access:  read_only
        .address_space:  global
        .offset:         128
        .size:           8
        .value_kind:     global_buffer
      - .actual_access:  write_only
        .address_space:  global
        .offset:         136
        .size:           8
        .value_kind:     global_buffer
      - .address_space:  global
        .offset:         144
        .size:           8
        .value_kind:     global_buffer
    .group_segment_fixed_size: 19456
    .kernarg_segment_align: 8
    .kernarg_segment_size: 152
    .language:       OpenCL C
    .language_version:
      - 2
      - 0
    .max_flat_workgroup_size: 256
    .name:           _Z7k_layerILi2EEvPKiS1_PKfS3_PKDF16_S3_S5_S5_PDF16_P15HIP_vector_typeIfLj4EES9_S3_S3_S3_S3_S3_S3_PfSA_
    .private_segment_fixed_size: 0
    .sgpr_count:     74
    .sgpr_spill_count: 0
    .symbol:         _Z7k_layerILi2EEvPKiS1_PKfS3_PKDF16_S3_S5_S5_PDF16_P15HIP_vector_typeIfLj4EES9_S3_S3_S3_S3_S3_S3_PfSA_.kd
    .uniform_work_group_size: 1
    .uses_dynamic_stack: false
    .vgpr_count:     110
    .vgpr_spill_count: 0
    .wavefront_size: 64
